# phase-6 B-fragment LDS addresses precomputed once (3 fewer instructions at the head of that load segment) in all four GEMM kernels
# speedup vs baseline: 1.0185x; 1.0078x over previous
.LBB2_32:
	s_xor_b64 s[30:31], s[4:5], -1
	s_lshl_b32 s4, s63, 8
	s_ashr_i32 s5, s4, 31
	s_lshl_b64 s[4:5], s[4:5], 11
	s_add_u32 s4, s14, s4
	s_addc_u32 s5, s15, s5
	s_add_u32 s24, s4, 0x400000
	s_addc_u32 s25, s5, 0
	s_and_b64 s[4:5], s[28:29], exec
	s_cselect_b32 s66, s25, s19
	s_cselect_b32 s67, s24, s18
	s_lshl_b32 s4, s62, 8
	s_ashr_i32 s5, s4, 31
	s_lshl_b64 s[4:5], s[4:5], 11
	s_add_u32 s26, s12, s4
	s_addc_u32 s27, s13, s5
	s_and_b64 s[4:5], s[28:29], exec
	s_cselect_b32 s68, s27, s1
	s_cselect_b32 s69, s26, s0
	s_add_u32 s70, s18, 0x40080
	s_addc_u32 s71, s19, 0
	s_add_u32 s72, s0, 0x100
	v_mov_b64_e32 v[0:1], 0
	s_addc_u32 s73, s1, 0
	s_mov_b32 s74, -2
	v_mov_b64_e32 v[2:3], 0
	v_mov_b64_e32 v[4:5], 0
	v_mov_b64_e32 v[6:7], 0
	v_mov_b64_e32 v[8:9], 0
	v_mov_b64_e32 v[10:11], 0
	v_mov_b64_e32 v[12:13], 0
	v_mov_b64_e32 v[14:15], 0
	v_mov_b64_e32 v[16:17], 0
	v_mov_b64_e32 v[18:19], 0
	v_mov_b64_e32 v[20:21], 0
	v_mov_b64_e32 v[22:23], 0
	v_mov_b64_e32 v[24:25], 0
	v_mov_b64_e32 v[26:27], 0
	v_mov_b64_e32 v[28:29], 0
	v_mov_b64_e32 v[30:31], 0
	v_mov_b64_e32 v[32:33], 0
	v_mov_b64_e32 v[34:35], 0
	v_mov_b64_e32 v[36:37], 0
	v_mov_b64_e32 v[38:39], 0
	v_mov_b64_e32 v[40:41], 0
	v_mov_b64_e32 v[42:43], 0
	v_mov_b64_e32 v[44:45], 0
	v_mov_b64_e32 v[46:47], 0
	v_mov_b64_e32 v[48:49], 0
	v_mov_b64_e32 v[50:51], 0
	v_mov_b64_e32 v[52:53], 0
	v_mov_b64_e32 v[54:55], 0
	v_mov_b64_e32 v[56:57], 0
	v_mov_b64_e32 v[58:59], 0
	v_mov_b64_e32 v[60:61], 0
	v_mov_b64_e32 v[62:63], 0
	v_mov_b64_e32 v[64:65], 0
	v_mov_b64_e32 v[66:67], 0
	v_mov_b64_e32 v[68:69], 0
	v_mov_b64_e32 v[70:71], 0
	v_mov_b64_e32 v[72:73], 0
	v_mov_b64_e32 v[74:75], 0
	v_mov_b64_e32 v[76:77], 0
	v_mov_b64_e32 v[78:79], 0
	v_mov_b64_e32 v[80:81], 0
	v_mov_b64_e32 v[82:83], 0
	v_mov_b64_e32 v[84:85], 0
	v_mov_b64_e32 v[86:87], 0
	v_mov_b64_e32 v[88:89], 0
	v_mov_b64_e32 v[90:91], 0
	v_mov_b64_e32 v[92:93], 0
	v_mov_b64_e32 v[94:95], 0
	v_mov_b64_e32 v[96:97], 0
	v_mov_b64_e32 v[98:99], 0
	v_mov_b64_e32 v[100:101], 0
	v_mov_b64_e32 v[102:103], 0
	v_mov_b64_e32 v[104:105], 0
	v_mov_b64_e32 v[106:107], 0
	v_mov_b64_e32 v[108:109], 0
	v_mov_b64_e32 v[110:111], 0
	v_mov_b64_e32 v[112:113], 0
	v_mov_b64_e32 v[114:115], 0
	v_mov_b64_e32 v[116:117], 0
	v_mov_b64_e32 v[118:119], 0
	v_mov_b64_e32 v[120:121], 0
	v_mov_b64_e32 v[122:123], 0
	v_mov_b64_e32 v[124:125], 0
	v_mov_b64_e32 v[126:127], 0
	s_waitcnt lgkmcnt(0)
	v_add_u32_e32 v212, 0x1c000, v199
	v_add_u32_e32 v213, 0x1c000, v200
	s_branch .LBB2_34

.LBB2_44:
	s_waitcnt lgkmcnt(8)
	s_barrier
	s_waitcnt lgkmcnt(0)
	s_setprio 1
	v_mfma_i32_16x16x64_i8 v[124:127], v[128:131], v[184:187], v[124:127]
	v_mfma_i32_16x16x64_i8 v[120:123], v[132:135], v[184:187], v[120:123]
	v_mfma_i32_16x16x64_i8 v[108:111], v[128:131], v[172:175], v[108:111]
	v_mfma_i32_16x16x64_i8 v[104:107], v[132:135], v[172:175], v[104:107]
	v_mfma_i32_16x16x64_i8 v[96:99], v[128:131], v[168:171], v[96:99]
	v_mfma_i32_16x16x64_i8 v[88:91], v[132:135], v[168:171], v[88:91]
	v_mfma_i32_16x16x64_i8 v[80:83], v[128:131], v[160:163], v[80:83]
	v_mfma_i32_16x16x64_i8 v[72:75], v[132:135], v[160:163], v[72:75]
	v_mfma_i32_16x16x64_i8 v[124:127], v[140:143], v[188:191], v[124:127]
	v_mfma_i32_16x16x64_i8 v[120:123], v[136:139], v[188:191], v[120:123]
	v_mfma_i32_16x16x64_i8 v[108:111], v[140:143], v[176:179], v[108:111]
	v_mfma_i32_16x16x64_i8 v[104:107], v[136:139], v[176:179], v[104:107]
	v_mfma_i32_16x16x64_i8 v[96:99], v[140:143], v[180:183], v[96:99]
	v_mfma_i32_16x16x64_i8 v[88:91], v[136:139], v[180:183], v[88:91]
	v_mfma_i32_16x16x64_i8 v[80:83], v[140:143], v[164:167], v[80:83]
	v_mfma_i32_16x16x64_i8 v[72:75], v[136:139], v[164:167], v[72:75]
	s_setprio 0
	s_barrier
	ds_read_b128 v[144:147], v212
	ds_read_b128 v[148:151], v212 offset:2048
	ds_read_b128 v[156:159], v213
	ds_read_b128 v[152:155], v213 offset:2048
	s_and_b64 vcc, exec, s[0:1]
	s_cbranch_vccnz .LBB2_46
	s_add_u32 s76, s16, 0x80
	s_addc_u32 s5, s75, 0
	s_and_b32 s77, s5, 0xffff
	s_mov_b32 s78, s6
	s_mov_b32 s79, s7
	s_mov_b32 m0, s47
	s_nop 0
	buffer_load_dwordx4 v196, s[76:79], 0 offen lds
	s_mov_b32 m0, s48
	s_nop 0
	buffer_load_dwordx4 v198, s[76:79], 0 offen lds

.Lp2_sum_skip:
	s_barrier
	buffer_load_dwordx4 v194, s[12:15], 0 offen lds
	s_mov_b32 m0, s41
	v_lshrrev_b32_e32 v2, 4, v0
	buffer_load_dwordx4 v196, s[12:15], 0 offen lds
	s_add_u32 s12, s16, 0x80
	s_addc_u32 s0, s9, 0
	s_add_i32 s42, s31, 0x8000
	s_and_b32 s13, s0, 0xffff
	s_mov_b32 m0, s42
	s_add_i32 s43, s31, 0xa000
	buffer_load_dwordx4 v1, s[12:15], 0 offen lds
	s_mov_b32 m0, s43
	v_and_b32_e32 v197, 15, v0
	buffer_load_dwordx4 v195, s[12:15], 0 offen lds
	s_add_u32 s12, s8, 0x10080
	s_addc_u32 s0, s25, 0
	s_add_i32 s44, s31, 0x1c000
	s_and_b32 s13, s0, 0xffff
	s_mov_b32 m0, s44
	s_add_i32 s45, s31, 0x1e000
	buffer_load_dwordx4 v194, s[12:15], 0 offen lds
	s_mov_b32 m0, s45
	s_and_b32 s0, s2, 1
	buffer_load_dwordx4 v196, s[12:15], 0 offen lds
	s_lshl_b32 s0, s0, 23
	s_lshl_b32 s1, s26, 21
	v_bfe_u32 v3, v0, 1, 3
	s_or_b32 s0, s0, s1
	v_bitop3_b32 v2, v2, v3, 3 bitop3:0x6c
	v_lshlrev_b32_e32 v3, 7, v197
	s_add_i32 s46, s31, 0xc000
	s_add_i32 s47, s31, 0xe000
	s_or_b32 s0, s27, s0
	v_lshlrev_b32_e32 v2, 4, v2
	v_lshl_or_b32 v4, s28, 13, v3
	v_lshl_or_b32 v3, s39, 12, v3
	s_waitcnt vmcnt(6)
	s_add_u32 s48, s20, s0
	v_or_b32_e32 v5, v4, v2
	v_bitop3_b32 v4, v4, 64, v2 bitop3:0x36
	v_or_b32_e32 v198, v3, v2
	v_bitop3_b32 v199, v3, 64, v2 bitop3:0x36
	s_addc_u32 s49, s21, 0
	v_mov_b32_e32 v66, 0
	s_add_i32 s0, 0, 0x10000
	s_add_i32 s1, 0, 0x14000
	s_mov_b32 s50, -2
	s_mov_b64 s[10:11], 0
	v_add_u32_e32 v200, 0, v5
	v_add_u32_e32 v201, 0, v4
	v_mov_b32_e32 v67, v66
	v_mov_b32_e32 v68, v66
	v_mov_b32_e32 v69, v66
	v_mov_b32_e32 v70, v66
	v_mov_b32_e32 v71, v66
	v_mov_b32_e32 v72, v66
	v_mov_b32_e32 v73, v66
	v_mov_b32_e32 v82, v66
	v_mov_b32_e32 v83, v66
	v_mov_b32_e32 v84, v66
	v_mov_b32_e32 v85, v66
	v_mov_b32_e32 v86, v66
	v_mov_b32_e32 v87, v66
	v_mov_b32_e32 v88, v66
	v_mov_b32_e32 v89, v66
	v_mov_b32_e32 v98, v66
	v_mov_b32_e32 v99, v66
	v_mov_b32_e32 v100, v66
	v_mov_b32_e32 v101, v66
	v_mov_b32_e32 v102, v66
	v_mov_b32_e32 v103, v66
	v_mov_b32_e32 v104, v66
	v_mov_b32_e32 v105, v66
	v_mov_b32_e32 v114, v66
	v_mov_b32_e32 v115, v66
	v_mov_b32_e32 v116, v66
	v_mov_b32_e32 v117, v66
	v_mov_b32_e32 v118, v66
	v_mov_b32_e32 v119, v66
	v_mov_b32_e32 v120, v66
	v_mov_b32_e32 v121, v66
	v_mov_b32_e32 v74, v66
	v_mov_b32_e32 v75, v66
	v_mov_b32_e32 v76, v66
	v_mov_b32_e32 v77, v66
	v_mov_b32_e32 v78, v66
	v_mov_b32_e32 v79, v66
	v_mov_b32_e32 v80, v66
	v_mov_b32_e32 v81, v66
	v_mov_b32_e32 v90, v66
	v_mov_b32_e32 v91, v66
	v_mov_b32_e32 v92, v66
	v_mov_b32_e32 v93, v66
	v_mov_b32_e32 v94, v66
	v_mov_b32_e32 v95, v66
	v_mov_b32_e32 v96, v66
	v_mov_b32_e32 v97, v66
	v_mov_b32_e32 v106, v66
	v_mov_b32_e32 v107, v66
	v_mov_b32_e32 v108, v66
	v_mov_b32_e32 v109, v66
	v_mov_b32_e32 v110, v66
	v_mov_b32_e32 v111, v66
	v_mov_b32_e32 v112, v66
	v_mov_b32_e32 v113, v66
	v_mov_b32_e32 v122, v66
	v_mov_b32_e32 v123, v66
	v_mov_b32_e32 v124, v66
	v_mov_b32_e32 v125, v66
	v_mov_b32_e32 v126, v66
	v_mov_b32_e32 v127, v66
	v_mov_b32_e32 v128, v66
	v_mov_b32_e32 v129, v66
	v_mov_b32_e32 v130, v66
	v_mov_b32_e32 v131, v66
	v_mov_b32_e32 v132, v66
	v_mov_b32_e32 v133, v66
	v_mov_b32_e32 v134, v66
	v_mov_b32_e32 v135, v66
	v_mov_b32_e32 v136, v66
	v_mov_b32_e32 v137, v66
	v_mov_b32_e32 v146, v66
	v_mov_b32_e32 v147, v66
	v_mov_b32_e32 v148, v66
	v_mov_b32_e32 v149, v66
	v_mov_b32_e32 v150, v66
	v_mov_b32_e32 v151, v66
	v_mov_b32_e32 v152, v66
	v_mov_b32_e32 v153, v66
	v_mov_b32_e32 v162, v66
	v_mov_b32_e32 v163, v66
	v_mov_b32_e32 v164, v66
	v_mov_b32_e32 v165, v66
	v_mov_b32_e32 v166, v66
	v_mov_b32_e32 v167, v66
	v_mov_b32_e32 v168, v66
	v_mov_b32_e32 v169, v66
	v_mov_b32_e32 v178, v66
	v_mov_b32_e32 v179, v66
	v_mov_b32_e32 v180, v66
	v_mov_b32_e32 v181, v66
	v_mov_b32_e32 v182, v66
	v_mov_b32_e32 v183, v66
	v_mov_b32_e32 v184, v66
	v_mov_b32_e32 v185, v66
	v_mov_b32_e32 v138, v66
	v_mov_b32_e32 v139, v66
	v_mov_b32_e32 v140, v66
	v_mov_b32_e32 v141, v66
	v_mov_b32_e32 v142, v66
	v_mov_b32_e32 v143, v66
	v_mov_b32_e32 v144, v66
	v_mov_b32_e32 v145, v66
	v_mov_b32_e32 v154, v66
	v_mov_b32_e32 v155, v66
	v_mov_b32_e32 v156, v66
	v_mov_b32_e32 v157, v66
	v_mov_b32_e32 v158, v66
	v_mov_b32_e32 v159, v66
	v_mov_b32_e32 v160, v66
	v_mov_b32_e32 v161, v66
	v_mov_b32_e32 v170, v66
	v_mov_b32_e32 v171, v66
	v_mov_b32_e32 v172, v66
	v_mov_b32_e32 v173, v66
	v_mov_b32_e32 v174, v66
	v_mov_b32_e32 v175, v66
	v_mov_b32_e32 v176, v66
	v_mov_b32_e32 v177, v66
	v_mov_b32_e32 v186, v66
	v_mov_b32_e32 v187, v66
	v_mov_b32_e32 v188, v66
	v_mov_b32_e32 v189, v66
	v_mov_b32_e32 v190, v66
	v_mov_b32_e32 v191, v66
	v_mov_b32_e32 v192, v66
	v_mov_b32_e32 v193, v66
	v_bfe_u32 v202, v0, 4, 2
	v_add_u32_e32 v203, s0, v198
	v_add_u32_e32 v204, s0, v199
	v_add_u32_e32 v205, s1, v198
	v_add_u32_e32 v206, s1, v199
	s_barrier
	s_cmpk_eq_i32 s10, 0x700
	s_cselect_b64 s[18:19], -1, 0
	s_cmpk_lg_i32 s10, 0x700
	s_cselect_b64 s[26:27], -1, 0
	s_add_u32 s54, s48, s10
	s_addc_u32 s55, s49, s11
	s_add_u32 s51, s8, s10
	s_addc_u32 s52, s25, s11
	s_add_u32 s20, s51, 0x100
	s_addc_u32 s53, s52, 0
	s_add_u32 s12, s54, 0x100080
	s_addc_u32 s0, s55, 0
	s_and_b32 s13, s0, 0xffff
	v_add_u32_e32 v210, 0x1c000, v198
	v_add_u32_e32 v211, 0x1c000, v199
	s_branch .LBB3_4

.LBB3_14:
	s_waitcnt lgkmcnt(8)
	s_barrier
	s_waitcnt lgkmcnt(0)
	s_setprio 1
	v_mfma_f32_16x16x128_f8f6f4 v[190:193], v[10:17], v[58:65], v[190:193]
	v_mfma_f32_16x16x128_f8f6f4 v[186:189], v[2:9], v[58:65], v[186:189]
	v_mfma_f32_16x16x128_f8f6f4 v[174:177], v[10:17], v[50:57], v[174:177]
	v_mfma_f32_16x16x128_f8f6f4 v[170:173], v[2:9], v[50:57], v[170:173]
	v_mfma_f32_16x16x128_f8f6f4 v[158:161], v[10:17], v[42:49], v[158:161]
	v_mfma_f32_16x16x128_f8f6f4 v[154:157], v[2:9], v[42:49], v[154:157]
	v_mfma_f32_16x16x128_f8f6f4 v[142:145], v[10:17], v[34:41], v[142:145]
	v_mfma_f32_16x16x128_f8f6f4 v[138:141], v[2:9], v[34:41], v[138:141]
	s_setprio 0
	s_barrier
	ds_read_b128 v[26:29], v210
	ds_read_b128 v[18:21], v210 offset:2048
	ds_read_b128 v[30:33], v211
	ds_read_b128 v[22:25], v211 offset:2048
	s_waitcnt vmcnt(8)
	s_and_b64 vcc, exec, s[0:1]
	s_cbranch_vccnz .LBB3_16
	s_and_b64 s[22:23], exec, s[18:19]
	s_cselect_b32 s20, s8, s20
	s_cselect_b32 s13, s25, s53
	s_add_u32 s56, s20, 0x80
	s_addc_u32 s13, s13, 0
	s_and_b32 s57, s13, 0xffff
	s_mov_b32 s58, s14
	s_mov_b32 s59, s15
	s_mov_b32 m0, s40
	s_nop 0
	buffer_load_dwordx4 v194, s[56:59], 0 offen lds
	s_mov_b32 m0, s41
	s_nop 0
	buffer_load_dwordx4 v196, s[56:59], 0 offen lds

	.amdhsa_kernel _ZN2rb6k_gemmILi1ENS_7SchedP2ENS_7EpiSlabEEEvT0_T1_
		.amdhsa_group_segment_fixed_size 0
		.amdhsa_private_segment_fixed_size 0
		.amdhsa_kernarg_size 40
		.amdhsa_user_sgpr_count 2
		.amdhsa_user_sgpr_dispatch_ptr 0
		.amdhsa_user_sgpr_queue_ptr 0
		.amdhsa_user_sgpr_kernarg_segment_ptr 1
		.amdhsa_user_sgpr_dispatch_id 0
		.amdhsa_user_sgpr_kernarg_preload_length 0
		.amdhsa_user_sgpr_kernarg_preload_offset 0
		.amdhsa_user_sgpr_private_segment_size 0
		.amdhsa_uses_dynamic_stack 0
		.amdhsa_enable_private_segment 0
		.amdhsa_system_sgpr_workgroup_id_x 1
		.amdhsa_system_sgpr_workgroup_id_y 0
		.amdhsa_system_sgpr_workgroup_id_z 0
		.amdhsa_system_sgpr_workgroup_info 0
		.amdhsa_system_vgpr_workitem_id 0
		.amdhsa_next_free_vgpr 212
		.amdhsa_next_free_sgpr 67
		.amdhsa_accum_offset 212
		.amdhsa_reserve_vcc 1
		.amdhsa_float_round_mode_32 0
		.amdhsa_float_round_mode_16_64 0
		.amdhsa_float_denorm_mode_32 3
		.amdhsa_float_denorm_mode_16_64 3
		.amdhsa_dx10_clamp 1
		.amdhsa_ieee_mode 1
		.amdhsa_fp16_overflow 0
		.amdhsa_tg_split 0
		.amdhsa_exception_fp_ieee_invalid_op 0
		.amdhsa_exception_fp_denorm_src 0
		.amdhsa_exception_fp_ieee_div_zero 0
		.amdhsa_exception_fp_ieee_overflow 0
		.amdhsa_exception_fp_ieee_underflow 0
		.amdhsa_exception_fp_ieee_inexact 0
		.amdhsa_exception_int_div_zero 0
	.end_amdhsa_kernel

.LBB4_12:
	s_and_b32 s33, s0, 3
	s_add_u32 s12, s8, 0x80
	s_addc_u32 s0, s3, 0
	s_add_i32 s36, s7, 0x18000
	s_and_b32 s13, s0, 0xffff
	s_mov_b32 m0, s36
	s_add_i32 s37, s7, 0x1a000
	s_waitcnt vmcnt(4)
	s_barrier
	buffer_load_dwordx4 v193, s[12:15], 0 offen lds
	s_mov_b32 m0, s37
	v_lshrrev_b32_e32 v1, 4, v0
	buffer_load_dwordx4 v195, s[12:15], 0 offen lds
	s_add_u32 s12, s16, 0x80
	s_addc_u32 s0, s9, 0
	s_add_i32 s38, s7, 0x8000
	s_and_b32 s13, s0, 0xffff
	s_mov_b32 m0, s38
	s_add_i32 s39, s7, 0xa000
	buffer_load_dwordx4 v192, s[12:15], 0 offen lds
	s_mov_b32 m0, s39
	v_and_b32_e32 v196, 15, v0
	buffer_load_dwordx4 v194, s[12:15], 0 offen lds
	s_add_u32 s12, s8, 0x4080
	s_addc_u32 s0, s3, 0
	s_add_i32 s40, s7, 0x1c000
	s_and_b32 s13, s0, 0xffff
	s_mov_b32 m0, s40
	s_add_i32 s41, s7, 0x1e000
	buffer_load_dwordx4 v193, s[12:15], 0 offen lds
	s_mov_b32 m0, s41
	v_bfe_u32 v197, v0, 4, 2
	buffer_load_dwordx4 v195, s[12:15], 0 offen lds
	v_bfe_u32 v0, v0, 1, 3
	v_bitop3_b32 v0, v1, v0, 3 bitop3:0x6c
	v_lshlrev_b32_e32 v1, 7, v196
	v_lshlrev_b32_e32 v0, 4, v0
	v_lshl_or_b32 v2, s27, 13, v1
	v_lshl_or_b32 v1, s33, 12, v1
	s_waitcnt vmcnt(6)
	v_or_b32_e32 v3, v2, v0
	v_or_b32_e32 v198, v1, v0
	v_bitop3_b32 v2, v2, 64, v0 bitop3:0x36
	v_bitop3_b32 v199, v1, 64, v0 bitop3:0x36
	v_mov_b32_e32 v64, 0
	s_add_i32 s0, 0, 0x10000
	s_add_i32 s1, 0, 0x14000
	s_add_i32 s42, s7, 0xc000
	s_add_i32 s43, s7, 0xe000
	s_mov_b32 s44, -2
	s_mov_b64 s[10:11], 0
	v_add_u32_e32 v200, 0, v3
	v_add_u32_e32 v201, 0, v2
	s_add_i32 s45, 0, 0x18000
	v_mov_b32_e32 v65, v64
	v_mov_b32_e32 v66, v64
	v_mov_b32_e32 v67, v64
	v_mov_b32_e32 v68, v64
	v_mov_b32_e32 v69, v64
	v_mov_b32_e32 v70, v64
	v_mov_b32_e32 v71, v64
	v_mov_b32_e32 v80, v64
	v_mov_b32_e32 v81, v64
	v_mov_b32_e32 v82, v64
	v_mov_b32_e32 v83, v64
	v_mov_b32_e32 v84, v64
	v_mov_b32_e32 v85, v64
	v_mov_b32_e32 v86, v64
	v_mov_b32_e32 v87, v64
	v_mov_b32_e32 v96, v64
	v_mov_b32_e32 v97, v64
	v_mov_b32_e32 v98, v64
	v_mov_b32_e32 v99, v64
	v_mov_b32_e32 v100, v64
	v_mov_b32_e32 v101, v64
	v_mov_b32_e32 v102, v64
	v_mov_b32_e32 v103, v64
	v_mov_b32_e32 v112, v64
	v_mov_b32_e32 v113, v64
	v_mov_b32_e32 v114, v64
	v_mov_b32_e32 v115, v64
	v_mov_b32_e32 v116, v64
	v_mov_b32_e32 v117, v64
	v_mov_b32_e32 v118, v64
	v_mov_b32_e32 v119, v64
	v_mov_b32_e32 v72, v64
	v_mov_b32_e32 v73, v64
	v_mov_b32_e32 v74, v64
	v_mov_b32_e32 v75, v64
	v_mov_b32_e32 v76, v64
	v_mov_b32_e32 v77, v64
	v_mov_b32_e32 v78, v64
	v_mov_b32_e32 v79, v64
	v_mov_b32_e32 v88, v64
	v_mov_b32_e32 v89, v64
	v_mov_b32_e32 v90, v64
	v_mov_b32_e32 v91, v64
	v_mov_b32_e32 v92, v64
	v_mov_b32_e32 v93, v64
	v_mov_b32_e32 v94, v64
	v_mov_b32_e32 v95, v64
	v_mov_b32_e32 v104, v64
	v_mov_b32_e32 v105, v64
	v_mov_b32_e32 v106, v64
	v_mov_b32_e32 v107, v64
	v_mov_b32_e32 v108, v64
	v_mov_b32_e32 v109, v64
	v_mov_b32_e32 v110, v64
	v_mov_b32_e32 v111, v64
	v_mov_b32_e32 v120, v64
	v_mov_b32_e32 v121, v64
	v_mov_b32_e32 v122, v64
	v_mov_b32_e32 v123, v64
	v_mov_b32_e32 v124, v64
	v_mov_b32_e32 v125, v64
	v_mov_b32_e32 v126, v64
	v_mov_b32_e32 v127, v64
	v_mov_b32_e32 v128, v64
	v_mov_b32_e32 v129, v64
	v_mov_b32_e32 v130, v64
	v_mov_b32_e32 v131, v64
	v_mov_b32_e32 v132, v64
	v_mov_b32_e32 v133, v64
	v_mov_b32_e32 v134, v64
	v_mov_b32_e32 v135, v64
	v_mov_b32_e32 v144, v64
	v_mov_b32_e32 v145, v64
	v_mov_b32_e32 v146, v64
	v_mov_b32_e32 v147, v64
	v_mov_b32_e32 v148, v64
	v_mov_b32_e32 v149, v64
	v_mov_b32_e32 v150, v64
	v_mov_b32_e32 v151, v64
	v_mov_b32_e32 v160, v64
	v_mov_b32_e32 v161, v64
	v_mov_b32_e32 v162, v64
	v_mov_b32_e32 v163, v64
	v_mov_b32_e32 v164, v64
	v_mov_b32_e32 v165, v64
	v_mov_b32_e32 v166, v64
	v_mov_b32_e32 v167, v64
	v_mov_b32_e32 v176, v64
	v_mov_b32_e32 v177, v64
	v_mov_b32_e32 v178, v64
	v_mov_b32_e32 v179, v64
	v_mov_b32_e32 v180, v64
	v_mov_b32_e32 v181, v64
	v_mov_b32_e32 v182, v64
	v_mov_b32_e32 v183, v64
	v_mov_b32_e32 v136, v64
	v_mov_b32_e32 v137, v64
	v_mov_b32_e32 v138, v64
	v_mov_b32_e32 v139, v64
	v_mov_b32_e32 v140, v64
	v_mov_b32_e32 v141, v64
	v_mov_b32_e32 v142, v64
	v_mov_b32_e32 v143, v64
	v_mov_b32_e32 v152, v64
	v_mov_b32_e32 v153, v64
	v_mov_b32_e32 v154, v64
	v_mov_b32_e32 v155, v64
	v_mov_b32_e32 v156, v64
	v_mov_b32_e32 v157, v64
	v_mov_b32_e32 v158, v64
	v_mov_b32_e32 v159, v64
	v_mov_b32_e32 v168, v64
	v_mov_b32_e32 v169, v64
	v_mov_b32_e32 v170, v64
	v_mov_b32_e32 v171, v64
	v_mov_b32_e32 v172, v64
	v_mov_b32_e32 v173, v64
	v_mov_b32_e32 v174, v64
	v_mov_b32_e32 v175, v64
	v_mov_b32_e32 v184, v64
	v_mov_b32_e32 v185, v64
	v_mov_b32_e32 v186, v64
	v_mov_b32_e32 v187, v64
	v_mov_b32_e32 v188, v64
	v_mov_b32_e32 v189, v64
	v_mov_b32_e32 v190, v64
	v_mov_b32_e32 v191, v64
	v_add_u32_e32 v202, s0, v198
	v_add_u32_e32 v203, s0, v199
	v_add_u32_e32 v204, s1, v198
	v_add_u32_e32 v205, s1, v199
	s_barrier
	s_cmpk_eq_i32 s10, 0x700
	s_cselect_b64 s[18:19], -1, 0
	s_cmpk_lg_i32 s10, 0x700
	s_cselect_b64 s[24:25], -1, 0
	s_add_u32 s49, s16, s10
	s_addc_u32 s50, s9, s11
	s_add_u32 s46, s8, s10
	s_addc_u32 s47, s3, s11
	s_add_u32 s20, s46, 0x100
	s_addc_u32 s48, s47, 0
	s_add_u32 s12, s49, 0x40080
	s_addc_u32 s0, s50, 0
	s_and_b32 s13, s0, 0xffff
	v_add_u32_e32 v207, 0x1c000, v198
	v_add_u32_e32 v208, 0x1c000, v199
	s_branch .LBB4_14

.LBB4_24:
	s_waitcnt lgkmcnt(8)
	s_barrier
	s_waitcnt lgkmcnt(0)
	s_setprio 1
	v_mfma_f32_16x16x128_f8f6f4 v[188:191], v[8:15], v[56:63], v[188:191]
	v_mfma_f32_16x16x128_f8f6f4 v[184:187], v[0:7], v[56:63], v[184:187]
	v_mfma_f32_16x16x128_f8f6f4 v[172:175], v[8:15], v[48:55], v[172:175]
	v_mfma_f32_16x16x128_f8f6f4 v[168:171], v[0:7], v[48:55], v[168:171]
	v_mfma_f32_16x16x128_f8f6f4 v[156:159], v[8:15], v[40:47], v[156:159]
	v_mfma_f32_16x16x128_f8f6f4 v[152:155], v[0:7], v[40:47], v[152:155]
	v_mfma_f32_16x16x128_f8f6f4 v[140:143], v[8:15], v[32:39], v[140:143]
	v_mfma_f32_16x16x128_f8f6f4 v[136:139], v[0:7], v[32:39], v[136:139]
	s_setprio 0
	s_barrier
	ds_read_b128 v[24:27], v207
	ds_read_b128 v[16:19], v207 offset:2048
	ds_read_b128 v[28:31], v208
	ds_read_b128 v[20:23], v208 offset:2048
	s_waitcnt vmcnt(8)
	s_and_b64 vcc, exec, s[0:1]
	s_cbranch_vccnz .LBB4_26
	s_and_b64 s[22:23], exec, s[18:19]
	s_cselect_b32 s20, s8, s20
	s_cselect_b32 s13, s3, s48
	s_add_u32 s48, s20, 0x80
	s_addc_u32 s13, s13, 0
	s_and_b32 s49, s13, 0xffff
	s_mov_b32 s50, s14
	s_mov_b32 s51, s15
	s_mov_b32 m0, s36
	s_nop 0
	buffer_load_dwordx4 v193, s[48:51], 0 offen lds
	s_mov_b32 m0, s37
	s_nop 0
	buffer_load_dwordx4 v195, s[48:51], 0 offen lds

	.amdhsa_kernel _ZN2rb6k_gemmILi1ENS_6SchedGILb1EEENS_5EpiP3EEEvT0_T1_
		.amdhsa_group_segment_fixed_size 0
		.amdhsa_private_segment_fixed_size 0
		.amdhsa_kernarg_size 48
		.amdhsa_user_sgpr_count 2
		.amdhsa_user_sgpr_dispatch_ptr 0
		.amdhsa_user_sgpr_queue_ptr 0
		.amdhsa_user_sgpr_kernarg_segment_ptr 1
		.amdhsa_user_sgpr_dispatch_id 0
		.amdhsa_user_sgpr_kernarg_preload_length 0
		.amdhsa_user_sgpr_kernarg_preload_offset 0
		.amdhsa_user_sgpr_private_segment_size 0
		.amdhsa_uses_dynamic_stack 0
		.amdhsa_enable_private_segment 0
		.amdhsa_system_sgpr_workgroup_id_x 1
		.amdhsa_system_sgpr_workgroup_id_y 0
		.amdhsa_system_sgpr_workgroup_id_z 0
		.amdhsa_system_sgpr_workgroup_info 0
		.amdhsa_system_vgpr_workitem_id 0
		.amdhsa_next_free_vgpr 209
		.amdhsa_next_free_sgpr 56
		.amdhsa_accum_offset 212
		.amdhsa_reserve_vcc 1
		.amdhsa_float_round_mode_32 0
		.amdhsa_float_round_mode_16_64 0
		.amdhsa_float_denorm_mode_32 3
		.amdhsa_float_denorm_mode_16_64 3
		.amdhsa_dx10_clamp 1
		.amdhsa_ieee_mode 1
		.amdhsa_fp16_overflow 0
		.amdhsa_tg_split 0
		.amdhsa_exception_fp_ieee_invalid_op 0
		.amdhsa_exception_fp_denorm_src 0
		.amdhsa_exception_fp_ieee_div_zero 0
		.amdhsa_exception_fp_ieee_overflow 0
		.amdhsa_exception_fp_ieee_underflow 0
		.amdhsa_exception_fp_ieee_inexact 0
		.amdhsa_exception_int_div_zero 0
	.end_amdhsa_kernel

.LBB5_16:
	s_and_b32 s35, s20, 3
	s_add_u32 s8, s12, 0x80
	s_load_dword s2, s[0:1], 0x48
	s_addc_u32 s0, s7, 0
	s_add_i32 s37, s25, 0x18000
	s_and_b32 s9, s0, 0xffff
	s_mov_b32 m0, s37
	s_add_i32 s38, s25, 0x1a000
	s_waitcnt vmcnt(4)
	s_barrier
	buffer_load_dwordx4 v192, s[8:11], 0 offen lds
	s_mov_b32 m0, s38
	v_lshrrev_b32_e32 v1, 4, v0
	buffer_load_dwordx4 v193, s[8:11], 0 offen lds
	s_add_u32 s8, s16, 0x80
	s_addc_u32 s0, s13, 0
	s_add_i32 s39, s25, 0x8000
	s_and_b32 s9, s0, 0xffff
	s_mov_b32 m0, s39
	s_add_i32 s40, s25, 0xa000
	buffer_load_dwordx4 v192, s[8:11], 0 offen lds
	s_mov_b32 m0, s40
	v_and_b32_e32 v194, 15, v0
	buffer_load_dwordx4 v193, s[8:11], 0 offen lds
	s_add_u32 s8, s12, 0x40080
	s_addc_u32 s0, s7, 0
	s_add_i32 s41, s25, 0x1c000
	s_and_b32 s9, s0, 0xffff
	s_mov_b32 m0, s41
	s_add_i32 s42, s25, 0x1e000
	buffer_load_dwordx4 v192, s[8:11], 0 offen lds
	s_mov_b32 m0, s42
	v_bfe_u32 v195, v0, 4, 2
	buffer_load_dwordx4 v193, s[8:11], 0 offen lds
	v_bfe_u32 v0, v0, 1, 3
	v_bitop3_b32 v0, v1, v0, 3 bitop3:0x6c
	v_lshlrev_b32_e32 v1, 7, v194
	v_lshlrev_b32_e32 v0, 4, v0
	v_lshl_or_b32 v2, s3, 13, v1
	v_lshl_or_b32 v1, s35, 12, v1
	s_waitcnt vmcnt(6)
	v_or_b32_e32 v3, v2, v0
	v_or_b32_e32 v196, v1, v0
	v_bitop3_b32 v2, v2, 64, v0 bitop3:0x36
	v_bitop3_b32 v197, v1, 64, v0 bitop3:0x36
	v_mov_b32_e32 v64, 0
	s_add_i32 s0, 0, 0x10000
	s_add_i32 s1, 0, 0x14000
	s_add_i32 s43, s25, 0xc000
	s_add_i32 s44, s25, 0xe000
	s_mov_b32 s45, -2
	s_mov_b64 s[14:15], 0
	v_add_u32_e32 v198, 0, v3
	v_add_u32_e32 v199, 0, v2
	s_add_i32 s46, 0, 0x18000
	v_mov_b32_e32 v65, v64
	v_mov_b32_e32 v66, v64
	v_mov_b32_e32 v67, v64
	v_mov_b32_e32 v68, v64
	v_mov_b32_e32 v69, v64
	v_mov_b32_e32 v70, v64
	v_mov_b32_e32 v71, v64
	v_mov_b32_e32 v76, v64
	v_mov_b32_e32 v77, v64
	v_mov_b32_e32 v78, v64
	v_mov_b32_e32 v79, v64
	v_mov_b32_e32 v80, v64
	v_mov_b32_e32 v81, v64
	v_mov_b32_e32 v82, v64
	v_mov_b32_e32 v83, v64
	v_mov_b32_e32 v88, v64
	v_mov_b32_e32 v89, v64
	v_mov_b32_e32 v90, v64
	v_mov_b32_e32 v91, v64
	v_mov_b32_e32 v92, v64
	v_mov_b32_e32 v93, v64
	v_mov_b32_e32 v94, v64
	v_mov_b32_e32 v95, v64
	v_mov_b32_e32 v104, v64
	v_mov_b32_e32 v105, v64
	v_mov_b32_e32 v106, v64
	v_mov_b32_e32 v107, v64
	v_mov_b32_e32 v108, v64
	v_mov_b32_e32 v109, v64
	v_mov_b32_e32 v110, v64
	v_mov_b32_e32 v111, v64
	v_mov_b32_e32 v72, v64
	v_mov_b32_e32 v73, v64
	v_mov_b32_e32 v74, v64
	v_mov_b32_e32 v75, v64
	v_mov_b32_e32 v84, v64
	v_mov_b32_e32 v85, v64
	v_mov_b32_e32 v86, v64
	v_mov_b32_e32 v87, v64
	v_mov_b32_e32 v96, v64
	v_mov_b32_e32 v97, v64
	v_mov_b32_e32 v98, v64
	v_mov_b32_e32 v99, v64
	v_mov_b32_e32 v100, v64
	v_mov_b32_e32 v101, v64
	v_mov_b32_e32 v102, v64
	v_mov_b32_e32 v103, v64
	v_mov_b32_e32 v112, v64
	v_mov_b32_e32 v113, v64
	v_mov_b32_e32 v114, v64
	v_mov_b32_e32 v115, v64
	v_mov_b32_e32 v116, v64
	v_mov_b32_e32 v117, v64
	v_mov_b32_e32 v118, v64
	v_mov_b32_e32 v119, v64
	v_mov_b32_e32 v120, v64
	v_mov_b32_e32 v121, v64
	v_mov_b32_e32 v122, v64
	v_mov_b32_e32 v123, v64
	v_mov_b32_e32 v124, v64
	v_mov_b32_e32 v125, v64
	v_mov_b32_e32 v126, v64
	v_mov_b32_e32 v127, v64
	v_mov_b32_e32 v128, v64
	v_mov_b32_e32 v129, v64
	v_mov_b32_e32 v130, v64
	v_mov_b32_e32 v131, v64
	v_mov_b32_e32 v132, v64
	v_mov_b32_e32 v133, v64
	v_mov_b32_e32 v134, v64
	v_mov_b32_e32 v135, v64
	v_mov_b32_e32 v140, v64
	v_mov_b32_e32 v141, v64
	v_mov_b32_e32 v142, v64
	v_mov_b32_e32 v143, v64
	v_mov_b32_e32 v148, v64
	v_mov_b32_e32 v149, v64
	v_mov_b32_e32 v150, v64
	v_mov_b32_e32 v151, v64
	v_mov_b32_e32 v156, v64
	v_mov_b32_e32 v157, v64
	v_mov_b32_e32 v158, v64
	v_mov_b32_e32 v159, v64
	v_mov_b32_e32 v164, v64
	v_mov_b32_e32 v165, v64
	v_mov_b32_e32 v166, v64
	v_mov_b32_e32 v167, v64
	v_mov_b32_e32 v172, v64
	v_mov_b32_e32 v173, v64
	v_mov_b32_e32 v174, v64
	v_mov_b32_e32 v175, v64
	v_mov_b32_e32 v180, v64
	v_mov_b32_e32 v181, v64
	v_mov_b32_e32 v182, v64
	v_mov_b32_e32 v183, v64
	v_mov_b32_e32 v136, v64
	v_mov_b32_e32 v137, v64
	v_mov_b32_e32 v138, v64
	v_mov_b32_e32 v139, v64
	v_mov_b32_e32 v144, v64
	v_mov_b32_e32 v145, v64
	v_mov_b32_e32 v146, v64
	v_mov_b32_e32 v147, v64
	v_mov_b32_e32 v152, v64
	v_mov_b32_e32 v153, v64
	v_mov_b32_e32 v154, v64
	v_mov_b32_e32 v155, v64
	v_mov_b32_e32 v160, v64
	v_mov_b32_e32 v161, v64
	v_mov_b32_e32 v162, v64
	v_mov_b32_e32 v163, v64
	v_mov_b32_e32 v168, v64
	v_mov_b32_e32 v169, v64
	v_mov_b32_e32 v170, v64
	v_mov_b32_e32 v171, v64
	v_mov_b32_e32 v176, v64
	v_mov_b32_e32 v177, v64
	v_mov_b32_e32 v178, v64
	v_mov_b32_e32 v179, v64
	v_mov_b32_e32 v184, v64
	v_mov_b32_e32 v185, v64
	v_mov_b32_e32 v186, v64
	v_mov_b32_e32 v187, v64
	v_mov_b32_e32 v188, v64
	v_mov_b32_e32 v189, v64
	v_mov_b32_e32 v190, v64
	v_mov_b32_e32 v191, v64
	v_add_u32_e32 v200, s0, v196
	v_add_u32_e32 v201, s0, v197
	v_add_u32_e32 v202, s1, v196
	v_add_u32_e32 v203, s1, v197
	s_barrier
	s_cmpk_eq_i32 s14, 0x700
	s_cselect_b64 s[18:19], -1, 0
	s_cmpk_lg_i32 s14, 0x700
	s_cselect_b64 s[26:27], -1, 0
	s_add_u32 s50, s16, s14
	s_addc_u32 s51, s13, s15
	s_add_u32 s47, s12, s14
	s_addc_u32 s48, s7, s15
	s_add_u32 s20, s47, 0x100
	s_addc_u32 s49, s48, 0
	s_add_u32 s8, s50, 0x40080
	s_addc_u32 s0, s51, 0
	s_and_b32 s9, s0, 0xffff
	v_add_u32_e32 v205, 0x1c000, v196
	v_add_u32_e32 v206, 0x1c000, v197
	s_branch .LBB5_18

.LBB5_28:
	s_waitcnt lgkmcnt(8)
	s_barrier
	s_waitcnt lgkmcnt(0)
	s_setprio 1
	v_mfma_f32_16x16x128_f8f6f4 v[188:191], v[8:15], v[56:63], v[188:191]
	v_mfma_f32_16x16x128_f8f6f4 v[184:187], v[0:7], v[56:63], v[184:187]
	v_mfma_f32_16x16x128_f8f6f4 v[176:179], v[8:15], v[48:55], v[176:179]
	v_mfma_f32_16x16x128_f8f6f4 v[168:171], v[0:7], v[48:55], v[168:171]
	v_mfma_f32_16x16x128_f8f6f4 v[160:163], v[8:15], v[40:47], v[160:163]
	v_mfma_f32_16x16x128_f8f6f4 v[152:155], v[0:7], v[40:47], v[152:155]
	v_mfma_f32_16x16x128_f8f6f4 v[144:147], v[8:15], v[32:39], v[144:147]
	v_mfma_f32_16x16x128_f8f6f4 v[136:139], v[0:7], v[32:39], v[136:139]
	s_setprio 0
	s_barrier
	ds_read_b128 v[24:27], v205
	ds_read_b128 v[16:19], v205 offset:2048
	ds_read_b128 v[28:31], v206
	ds_read_b128 v[20:23], v206 offset:2048
	s_waitcnt vmcnt(8)
	s_and_b64 vcc, exec, s[0:1]
	s_cbranch_vccnz .LBB5_30
	s_and_b64 s[22:23], exec, s[18:19]
	s_cselect_b32 s20, s12, s20
	s_cselect_b32 s9, s7, s49
	s_add_u32 s52, s20, 0x80
	s_addc_u32 s9, s9, 0
	s_and_b32 s53, s9, 0xffff
	s_mov_b32 s54, s10
	s_mov_b32 s55, s11
	s_mov_b32 m0, s37
	s_nop 0
	buffer_load_dwordx4 v192, s[52:55], 0 offen lds
	s_mov_b32 m0, s38
	s_nop 0
	buffer_load_dwordx4 v193, s[52:55], 0 offen lds

	.amdhsa_kernel _ZN2rb6k_gemmILi1ENS_6SchedGILb1EEENS_6EpiOutEEEvT0_T1_
		.amdhsa_group_segment_fixed_size 0
		.amdhsa_private_segment_fixed_size 0
		.amdhsa_kernarg_size 80
		.amdhsa_user_sgpr_count 2
		.amdhsa_user_sgpr_dispatch_ptr 0
		.amdhsa_user_sgpr_queue_ptr 0
		.amdhsa_user_sgpr_kernarg_segment_ptr 1
		.amdhsa_user_sgpr_dispatch_id 0
		.amdhsa_user_sgpr_kernarg_preload_length 0
		.amdhsa_user_sgpr_kernarg_preload_offset 0
		.amdhsa_user_sgpr_private_segment_size 0
		.amdhsa_uses_dynamic_stack 0
		.amdhsa_enable_private_segment 0
		.amdhsa_system_sgpr_workgroup_id_x 1
		.amdhsa_system_sgpr_workgroup_id_y 0
		.amdhsa_system_sgpr_workgroup_id_z 0
		.amdhsa_system_sgpr_workgroup_info 0
		.amdhsa_system_vgpr_workitem_id 0
		.amdhsa_next_free_vgpr 207
		.amdhsa_next_free_sgpr 56
		.amdhsa_accum_offset 208
		.amdhsa_reserve_vcc 1
		.amdhsa_float_round_mode_32 0
		.amdhsa_float_round_mode_16_64 0
		.amdhsa_float_denorm_mode_32 3
		.amdhsa_float_denorm_mode_16_64 3
		.amdhsa_dx10_clamp 1
		.amdhsa_ieee_mode 1
		.amdhsa_fp16_overflow 0
		.amdhsa_tg_split 0
		.amdhsa_exception_fp_ieee_invalid_op 0
		.amdhsa_exception_fp_denorm_src 0
		.amdhsa_exception_fp_ieee_div_zero 0
		.amdhsa_exception_fp_ieee_overflow 0
		.amdhsa_exception_fp_ieee_underflow 0
		.amdhsa_exception_fp_ieee_inexact 0
		.amdhsa_exception_int_div_zero 0
	.end_amdhsa_kernel

amdhsa.kernels:
  - .agpr_count:     0
    .args:
      - .actual_access:  read_only
        .address_space:  global
        .offset:         0
        .size:           8
        .value_kind:     global_buffer
      - .actual_access:  read_only
        .address_space:  global
        .offset:         8
        .size:           8
        .value_kind:     global_buffer
      - .actual_access:  read_only
        .address_space:  global
        .offset:         16
        .size:           8
        .value_kind:     global_buffer
      - .actual_access:  read_only
        .address_space:  global
        .offset:         24
        .size:           8
        .value_kind:     global_buffer
      - .actual_access:  read_only
        .address_space:  global
        .offset:         32
        .size:           8
        .value_kind:     global_buffer
      - .actual_access:  read_only
        .address_space:  global
        .offset:         40
        .size:           8
        .value_kind:     global_buffer
      - .actual_access:  read_only
        .address_space:  global
        .offset:         48
        .size:           8
        .value_kind:     global_buffer
      - .actual_access:  read_only
        .address_space:  global
        .offset:         56
        .size:           8
        .value_kind:     global_buffer
      - .actual_access:  write_only
        .address_space:  global
        .offset:         64
        .size:           8
        .value_kind:     global_buffer
      - .offset:         72
        .size:           4
        .value_kind:     by_value
    .group_segment_fixed_size: 32768
    .kernarg_segment_align: 8
    .kernarg_segment_size: 76
    .language:       OpenCL C
    .language_version:
      - 2
      - 0
    .max_flat_workgroup_size: 256
    .name:           _ZN2rb6k_prepEPKfS1_S1_S1_S1_S1_S1_S1_Phi
    .private_segment_fixed_size: 0
    .sgpr_count:     22
    .sgpr_spill_count: 0
    .symbol:         _ZN2rb6k_prepEPKfS1_S1_S1_S1_S1_S1_S1_Phi.kd
    .uniform_work_group_size: 1
    .uses_dynamic_stack: false
    .vgpr_count:     100
    .vgpr_spill_count: 0
    .wavefront_size: 64
  - .agpr_count:     0
    .args:
      - .address_space:  global
        .offset:         0
        .size:           8
        .value_kind:     global_buffer
      - .actual_access:  read_only
        .address_space:  global
        .offset:         8
        .size:           8
        .value_kind:     global_buffer
    .group_segment_fixed_size: 0
    .kernarg_segment_align: 8
    .kernarg_segment_size: 16
    .language:       OpenCL C
    .language_version:
      - 2
      - 0
    .max_flat_workgroup_size: 256
    .name:           _ZN2rb5k_midEPhPKf
    .private_segment_fixed_size: 0
    .sgpr_count:     20
    .sgpr_spill_count: 0
    .symbol:         _ZN2rb5k_midEPhPKf.kd
    .uniform_work_group_size: 1
    .uses_dynamic_stack: false
    .vgpr_count:     86
    .vgpr_spill_count: 0
    .wavefront_size: 64
  - .agpr_count:     0
    .args:
      - .offset:         0
        .size:           24
        .value_kind:     by_value
      - .offset:         24
        .size:           64
        .value_kind:     by_value
    .group_segment_fixed_size: 0
    .kernarg_segment_align: 8
    .kernarg_segment_size: 88
    .language:       OpenCL C
    .language_version:
      - 2
      - 0
    .max_flat_workgroup_size: 512
    .name:           _ZN2rb6k_gemmILi2ENS_7SchedP1ENS_5EpiP1EEEvT0_T1_
    .private_segment_fixed_size: 0
    .sgpr_count:     86
    .sgpr_spill_count: 0
    .symbol:         _ZN2rb6k_gemmILi2ENS_7SchedP1ENS_5EpiP1EEEvT0_T1_.kd
    .uniform_work_group_size: 1
    .uses_dynamic_stack: false
    .vgpr_count:     214
    .vgpr_spill_count: 0
    .wavefront_size: 64
  - .agpr_count:     0
    .args:
      - .offset:         0
        .size:           24
        .value_kind:     by_value
      - .offset:         24
        .size:           16
        .value_kind:     by_value
    .group_segment_fixed_size: 0
    .kernarg_segment_align: 8
    .kernarg_segment_size: 40
    .language:       OpenCL C
    .language_version:
      - 2
      - 0
    .max_flat_workgroup_size: 512
    .name:           _ZN2rb6k_gemmILi1ENS_7SchedP2ENS_7EpiSlabEEEvT0_T1_
    .private_segment_fixed_size: 0
    .sgpr_count:     73
    .sgpr_spill_count: 0
    .symbol:         _ZN2rb6k_gemmILi1ENS_7SchedP2ENS_7EpiSlabEEEvT0_T1_.kd
    .uniform_work_group_size: 1
    .uses_dynamic_stack: false
    .vgpr_count:     212
    .vgpr_spill_count: 0
    .wavefront_size: 64
  - .agpr_count:     0
    .args:
      - .offset:         0
        .size:           32
        .value_kind:     by_value
      - .offset:         32
        .size:           16
        .value_kind:     by_value
    .group_segment_fixed_size: 0
    .kernarg_segment_align: 8
    .kernarg_segment_size: 48
    .language:       OpenCL C
    .language_version:
      - 2
      - 0
    .max_flat_workgroup_size: 512
    .name:           _ZN2rb6k_gemmILi1ENS_6SchedGILb1EEENS_5EpiP3EEEvT0_T1_
    .private_segment_fixed_size: 0
    .sgpr_count:     62
    .sgpr_spill_count: 0
    .symbol:         _ZN2rb6k_gemmILi1ENS_6SchedGILb1EEENS_5EpiP3EEEvT0_T1_.kd
    .uniform_work_group_size: 1
    .uses_dynamic_stack: false
    .vgpr_count:     209
    .vgpr_spill_count: 0
    .wavefront_size: 64
  - .agpr_count:     0
    .args:
      - .offset:         0
        .size:           32
        .value_kind:     by_value
      - .offset:         32
        .size:           48
        .value_kind:     by_value
    .group_segment_fixed_size: 0
    .kernarg_segment_align: 8
    .kernarg_segment_size: 80
    .language:       OpenCL C
    .language_version:
      - 2
      - 0
    .max_flat_workgroup_size: 512
    .name:           _ZN2rb6k_gemmILi1ENS_6SchedGILb1EEENS_6EpiOutEEEvT0_T1_
    .private_segment_fixed_size: 0
    .sgpr_count:     62
    .sgpr_spill_count: 0
    .symbol:         _ZN2rb6k_gemmILi1ENS_6SchedGILb1EEENS_6EpiOutEEEvT0_T1_.kd
    .uniform_work_group_size: 1
    .uses_dynamic_stack: false
    .vgpr_count:     207
    .vgpr_spill_count: 0
    .wavefront_size: 64
  - .agpr_count:     0
    .args:
      - .offset:         0
        .size:           24
        .value_kind:     by_value
      - .offset:         24
        .size:           1
        .value_kind:     by_value
    .group_segment_fixed_size: 0
    .kernarg_segment_align: 8
    .kernarg_segment_size: 28
    .language:       OpenCL C
    .language_version:
      - 2
      - 0
    .max_flat_workgroup_size: 512
    .name:           _ZN2rb6k_gemmILi2ENS_7SchedP1ENS_7EpiNullEEEvT0_T1_
    .private_segment_fixed_size: 0
    .sgpr_count:     66
    .sgpr_spill_count: 0
    .symbol:         _ZN2rb6k_gemmILi2ENS_7SchedP1ENS_7EpiNullEEEvT0_T1_.kd
    .uniform_work_group_size: 1
    .uses_dynamic_stack: false
    .vgpr_count:     205
    .vgpr_spill_count: 0
    .wavefront_size: 64
